# P4 conv_task: task id permuted within each wave (channel groups fastest) so ds_write_b128 lane groups hit distinct LDS banks, on top of v63
# speedup vs baseline: 1.0205x; 1.0045x over previous
; __device__ __forceinline__ void ssd_tables(const Params& p, LAS float* dtl, LAS float* csl, LAS float* wtot, size_t trow0, int h0, int nh, int lane, int wave) {
;     ...
;         dtl[hh * 128 + l] = dt; csl[hh * 128 + l] = v;
;     }
;     __syncthreads();
; __device__ __forceinline__ void phase_ssd_out(const Params& p, LAS unsigned char* lds, int G, int lane, int wave) {
;     ...
;         int tq = threadIdx.x; asm volatile("" : "+v"(tq));
;         for (int task = tq; task < 64 * 16; task += NTHREADS) { const int cg = task >> 4, run = task & 15;
;             if (cg < 16) conv_task<false, false>(p, proj, trow0, tl0, run, 1280 + g * 128 + cg * 8, Cs, cg * 8, nullptr);
;             else if (cg < 32) conv_task<false, false>(p, proj, trow0, tl0, run, 1024 + g * 128 + (cg - 16) * 8, Bs, (cg - 16) * 8, nullptr);
.LBB0_442:
	s_lshl_b32 s0, s39, 9
	s_addk_i32 s0, 0x800
	v_lshl_or_b32 v1, v1, 2, s0
	v_add_u32_e32 v1, 0, v1
	v_add_u32_e32 v4, 0x22000, v1
	v_add_u32_e32 v1, 0x23000, v1
	ds_write_b32 v1, v3
	v_bfe_u32 v246, v0, 2, 4
	v_and_b32_e32 v1, 3, v0
	v_lshl_or_b32 v1, v1, 4, v246
	v_and_b32_e32 v246, 0xffffffc0, v0
	v_or_b32_e32 v1, v1, v246
	s_movk_i32 s0, 0x400
	ds_write_b32 v4, v2
	s_waitcnt lgkmcnt(0)
	s_barrier
	s_mul_i32 s14, s37, 0x1e00
	v_cmp_gt_i32_e32 vcc, s0, v1
	s_and_saveexec_b64 s[4:5], vcc
	s_cbranch_execz .LBB0_471
	v_and_b32_e32 v4, 15, v1
	v_lshl_or_b32 v5, v4, 3, s36
	v_mov_b64_e32 v[2:3], s[18:19]
	v_mad_u64_u32 v[2:3], s[0:1], v5, s76, v[2:3]
	v_add_u32_e32 v3, s14, v3
	s_lshl_b32 s47, s38, 7
	v_lshl_add_u64 v[82:83], v[2:3], 0, s[58:59]
	v_or_b32_e32 v2, s17, v4
	s_movk_i32 s6, 0x880
	s_lshl_b32 s15, s38, 9
	s_or_b32 s46, s47, 0x500
	v_cmp_ne_u32_e64 s[0:1], 0, v2
	v_lshl_add_u32 v84, v4, 4, s77
	v_mad_u32_u24 v85, v4, s6, 0
	s_addk_i32 s47, 0x380
	s_mov_b64 s[6:7], 0
	s_branch .LBB0_446

; #define LAS __attribute__((address_space(3)))
; __device__ __forceinline__ void unpack8(const v4u q, float (&d)[8]) { d[0] = bflo(q.x); d[1] = bfhi(q.x); d[2] = bflo(q.y); d[3] = bfhi(q.y); d[4] = bflo(q.z); d[5] = bfhi(q.z); d[6] = bflo(q.w); d[7] = bfhi(q.w); }
; template <bool TR, bool SCALE>
; __device__ __forceinline__ void conv_task(const Params& p, const bf16* proj, size_t trow0, int tl0, int run, int xcol, LAS bf16* dst, int d0, const LAS float* sc) {
;     float w[4][8], bb[8];
; #pragma unroll
;     for (int k = 0; k < 4; ++k) { const f32x4 a = *(const f32x4*)(p.conv_w + k * NXBC + xcol), b = *(const f32x4*)(p.conv_w + k * NXBC + xcol + 4);
;         w[k][0] = a[0]; w[k][1] = a[1]; w[k][2] = a[2]; w[k][3] = a[3]; w[k][4] = b[0]; w[k][5] = b[1]; w[k][6] = b[2]; w[k][7] = b[3]; }
;     { const f32x4 a = *(const f32x4*)(p.conv_b + xcol), b = *(const f32x4*)(p.conv_b + xcol + 4); bb[0] = a[0]; bb[1] = a[1]; bb[2] = a[2]; bb[3] = a[3]; bb[4] = b[0]; bb[5] = b[1]; bb[6] = b[2]; bb[7] = b[3]; }
;     const int l0 = run * 8; const bf16* src = proj + (trow0 + l0) * PROJ_LD + COL_XBC + xcol;
;     float r0[8], r1[8], r2[8];
;     { const int pos = tl0 + l0; v4u q0 = (v4u){0u, 0u, 0u, 0u}, q1 = q0, q2 = q0;
;       if (pos - 3 >= 0) q0 = *(const v4u*)(src - 3 * PROJ_LD);
;       if (pos - 2 >= 0) q1 = *(const v4u*)(src - 2 * PROJ_LD);
;       if (pos - 1 >= 0) q2 = *(const v4u*)(src - 1 * PROJ_LD);
;       unpack8(q0, r0); unpack8(q1, r1); unpack8(q2, r2); }
; __device__ __forceinline__ void phase_ssd_out(const Params& p, LAS unsigned char* lds, int G, int lane, int wave) {
;     ...
;         { int tz_ = threadIdx.x; asm volatile("" : "+v"(tz_)); const int cg = tz_ >> 4, run = tz_ & 15; conv_task<true, false>(p, proj, trow0, tl0, run, (h0 + 4) * 64 + cg * 8, XT, cg * 8, nullptr); }
.LBB0_487:
	s_or_b64 exec, exec, s[0:1]
	v_bfe_u32 v246, v0, 2, 4
	v_and_b32_e32 v44, 3, v0
	v_lshl_or_b32 v44, v44, 4, v246
	v_and_b32_e32 v246, 0xffffffc0, v0
	v_or_b32_e32 v44, v44, v246
	s_waitcnt lgkmcnt(0)
	s_barrier
	s_or_b32 s8, s16, 4
	v_ashrrev_i32_e32 v1, 1, v44
	v_and_b32_e32 v1, -8, v1
	v_lshl_add_u32 v42, s8, 6, v1
	v_ashrrev_i32_e32 v43, 31, v42
	v_lshlrev_b64 v[18:19], 2, v[42:43]
	v_lshl_add_u64 v[14:15], s[84:85], 0, v[18:19]
	v_add_co_u32_e32 v8, vcc, s78, v14
	s_movk_i32 s0, 0x4000
	s_nop 0
	v_addc_co_u32_e32 v9, vcc, 0, v15, vcc
	v_add_co_u32_e32 v12, vcc, s79, v14
	global_load_dwordx4 v[2:5], v[14:15], off offset:16
	global_load_dwordx4 v[22:25], v[14:15], off
	v_addc_co_u32_e32 v13, vcc, 0, v15, vcc
	v_lshl_add_u64 v[6:7], v[14:15], 0, s[26:27]
	v_lshl_add_u64 v[10:11], v[14:15], 0, s[28:29]
	v_lshl_add_u64 v[16:17], v[14:15], 0, s[30:31]
	v_add_co_u32_e32 v14, vcc, s0, v14
	v_lshl_add_u64 v[38:39], s[86:87], 0, v[18:19]
	s_nop 0
	v_addc_co_u32_e32 v15, vcc, 0, v15, vcc
	global_load_dwordx4 v[26:29], v[8:9], off offset:2048
	s_nop 0
	global_load_dwordx4 v[6:9], v[6:7], off offset:16
	s_nop 0
	global_load_dwordx4 v[30:33], v[12:13], off
	s_nop 0
	global_load_dwordx4 v[10:13], v[10:11], off offset:16
	s_nop 0
	global_load_dwordx4 v[34:37], v[14:15], off offset:2048
	s_nop 0
	global_load_dwordx4 v[14:17], v[16:17], off offset:16
	s_nop 0
	global_load_dwordx4 v[18:21], v[38:39], off offset:16
	s_nop 0
	global_load_dwordx4 v[38:41], v[38:39], off
	v_lshlrev_b32_e32 v44, 3, v44
	v_and_b32_e32 v54, 0x78, v44
	v_or_b32_e32 v46, s36, v54
	v_mov_b64_e32 v[44:45], s[18:19]
	v_mad_u64_u32 v[44:45], s[0:1], v46, s76, v[44:45]
	v_add_u32_e32 v45, s14, v45
	v_lshl_add_u64 v[42:43], v[42:43], 1, v[44:45]
	v_lshl_add_u64 v[80:81], v[42:43], 0, s[58:59]
	v_or_b32_e32 v43, s17, v54
	v_mov_b32_e32 v42, 0
	v_cmp_ne_u32_e64 s[0:1], 0, v43
	v_mov_b32_e32 v46, 0
	v_mov_b32_e32 v47, 0
	v_mov_b32_e32 v48, 0
	v_mov_b32_e32 v49, 0
	s_and_saveexec_b64 s[6:7], s[0:1]
	s_cbranch_execz .LBB0_489
	v_add_co_u32_e32 v44, vcc, 0xffffb000, v80
	s_nop 1
	v_addc_co_u32_e32 v45, vcc, -1, v81, vcc
	global_load_dwordx4 v[46:49], v[44:45], off offset:-2560
